# speedup vs baseline: 1.0268x; 1.0024x over previous
.LBB1_3:
	s_load_dwordx8 s[4:11], s[0:1], 0x0
	v_lshrrev_b32_e32 v1, 6, v0
	v_mov_b32_e32 v3, 0
	v_lshl_or_b32 v2, s2, 2, v1
	v_lshlrev_b32_e32 v7, 12, v2
	s_waitcnt lgkmcnt(0)
	v_lshl_add_u64 v[4:5], v[2:3], 2, s[4:5]
	global_load_dword v6, v[4:5], off
	v_and_b32_e32 v8, 0x3ff000, v7
	v_and_b32_e32 v1, 63, v0
	v_mov_b32_e32 v9, v3
	v_lshlrev_b32_e32 v4, 4, v1
	v_mov_b32_e32 v5, v3
	v_lshl_add_u64 v[8:9], s[8:9], 0, v[8:9]
	v_lshl_add_u64 v[38:39], v[8:9], 0, v[4:5]
	s_mov_b32 s3, 0xf800000
	v_mov_b32_e32 v78, 0x260
	s_waitcnt vmcnt(0)
	v_ashrrev_i32_e32 v7, 31, v6
	v_lshlrev_b64 v[6:7], 12, v[6:7]
	v_lshl_add_u64 v[6:7], s[6:7], 0, v[6:7]
	v_lshl_add_u64 v[40:41], v[6:7], 0, v[4:5]
	global_load_dwordx4 v[6:9], v[40:41], off
	global_load_dwordx4 v[10:13], v[38:39], off
	global_load_dwordx4 v[14:17], v[38:39], off offset:1024
	global_load_dwordx4 v[18:21], v[40:41], off offset:1024
	global_load_dwordx4 v[22:25], v[40:41], off offset:2048
	global_load_dwordx4 v[26:29], v[38:39], off offset:2048
	global_load_dwordx4 v[30:33], v[38:39], off offset:3072
	global_load_dwordx4 v[34:37], v[40:41], off offset:3072
	v_mbcnt_lo_u32_b32 v38, -1, 0
	v_mbcnt_hi_u32_b32 v38, -1, v38
	v_and_b32_e32 v39, 64, v38
	v_xor_b32_e32 v40, 32, v38
	v_add_u32_e32 v39, 64, v39
	v_cmp_lt_i32_e32 vcc, v40, v39
	s_load_dwordx4 s[4:7], s[0:1], 0x20
	s_load_dwordx2 s[8:9], s[0:1], 0x30
	v_cndmask_b32_e32 v40, v38, v40, vcc
	v_lshlrev_b32_e32 v70, 2, v40
	s_waitcnt vmcnt(6)
	v_pk_add_f32 v[6:7], v[6:7], v[10:11]
	v_pk_add_f32 v[8:9], v[8:9], v[12:13]
	s_waitcnt vmcnt(4)
	v_pk_add_f32 v[10:11], v[18:19], v[14:15]
	v_pk_add_f32 v[12:13], v[20:21], v[16:17]
	s_waitcnt vmcnt(2)
	v_pk_add_f32 v[14:15], v[22:23], v[26:27]
	v_pk_add_f32 v[16:17], v[24:25], v[28:29]
	v_mov_b32_e32 v22, v6
	v_mov_b32_e32 v23, v8
	v_mov_b32_e32 v24, v7
	v_mov_b32_e32 v25, v9
	v_mov_b32_e32 v26, v10
	v_mov_b32_e32 v27, v12
	v_mov_b32_e32 v28, v11
	v_mov_b32_e32 v29, v13
	v_pk_add_f32 v[22:23], v[22:23], v[24:25]
	v_pk_add_f32 v[24:25], v[26:27], v[28:29]
	s_waitcnt vmcnt(0)
	v_pk_add_f32 v[18:19], v[34:35], v[30:31]
	v_pk_add_f32 v[20:21], v[36:37], v[32:33]
	v_pk_add_f32 v[30:31], v[14:15], v[14:15] op_sel:[0,1] op_sel_hi:[1,0]
	v_pk_add_f32 v[32:33], v[16:17], v[16:17] op_sel:[0,1] op_sel_hi:[1,0]
	v_add_f32_e32 v26, v22, v23
	v_pk_add_f32 v[22:23], v[24:25], v[24:25] op_sel:[0,1] op_sel_hi:[1,0]
	v_mov_b32_e32 v35, v18
	v_mov_b32_e32 v31, v20
	v_mov_b32_e32 v33, v21
	v_add_f32_e32 v34, 0, v26
	v_mov_b32_e32 v23, v19
	v_pk_add_f32 v[24:25], v[30:31], v[32:33]
	v_pk_add_f32 v[22:23], v[34:35], v[22:23]
	s_nop 0
	v_pk_add_f32 v[22:23], v[22:23], v[24:25]
	v_xor_b32_e32 v24, 16, v38
	v_add_f32_e32 v22, v22, v23
	v_mov_b32_e32 v23, v22
	v_cmp_lt_i32_e32 vcc, v24, v39
	s_waitcnt lgkmcnt(0)
	s_nop 1
	v_permlane32_swap_b32_e32 v22, v23
	v_add_f32_e32 v22, v22, v23
	v_cndmask_b32_e32 v24, v38, v24, vcc
	v_lshlrev_b32_e32 v71, 2, v24
	v_mov_b32_e32 v23, v22
	v_xor_b32_e32 v24, 8, v38
	v_cmp_lt_i32_e32 vcc, v24, v39
	s_waitcnt lgkmcnt(0)
	s_nop 1
	v_permlane16_swap_b32_e32 v22, v23
	v_add_f32_e32 v22, v22, v23
	v_cndmask_b32_e32 v24, v38, v24, vcc
	v_lshlrev_b32_e32 v72, 2, v24
	v_xor_b32_e32 v24, 4, v38
	v_cmp_lt_i32_e32 vcc, v24, v39
	s_waitcnt lgkmcnt(0)
	s_nop 1
	v_add_f32_dpp v22, v22, v22 row_ror:8 row_mask:0xf bank_mask:0xf
	v_cndmask_b32_e32 v24, v38, v24, vcc
	v_lshlrev_b32_e32 v73, 2, v24
	v_xor_b32_e32 v24, 2, v38
	v_cmp_lt_i32_e32 vcc, v24, v39
	s_waitcnt lgkmcnt(0)
	s_nop 1
	v_add_f32_dpp v22, v22, v22 row_ror:4 row_mask:0xf bank_mask:0xf
	v_cndmask_b32_e32 v24, v38, v24, vcc
	v_lshlrev_b32_e32 v74, 2, v24
	v_xor_b32_e32 v24, 1, v38
	v_cmp_lt_i32_e32 vcc, v24, v39
	s_nop 1
	v_cndmask_b32_e32 v24, v38, v24, vcc
	v_lshlrev_b32_e32 v75, 2, v24
	s_waitcnt lgkmcnt(0)
	s_nop 1
	v_add_f32_dpp v38, v22, v22 row_ror:2 row_mask:0xf bank_mask:0xf
	global_load_dwordx4 v[22:25], v4, s[4:5]
	global_load_dwordx4 v[26:29], v4, s[6:7]
	global_load_dwordx4 v[30:33], v4, s[4:5] offset:1024
	global_load_dwordx4 v[34:37], v4, s[6:7] offset:1024
	s_waitcnt lgkmcnt(0)
	s_nop 1
	v_add_f32_dpp v38, v38, v38 row_ror:1 row_mask:0xf bank_mask:0xf
	v_mul_f32_e32 v38, 0x3a800000, v38
	v_pk_add_f32 v[54:55], v[6:7], v[38:39] op_sel_hi:[1,0] neg_lo:[0,1] neg_hi:[0,1]
	v_pk_add_f32 v[56:57], v[8:9], v[38:39] op_sel_hi:[1,0] neg_lo:[0,1] neg_hi:[0,1]
	v_pk_add_f32 v[58:59], v[10:11], v[38:39] op_sel_hi:[1,0] neg_lo:[0,1] neg_hi:[0,1]
	v_pk_add_f32 v[60:61], v[12:13], v[38:39] op_sel_hi:[1,0] neg_lo:[0,1] neg_hi:[0,1]
	v_mov_b32_e32 v40, v55
	v_mov_b32_e32 v41, v57
	v_mov_b32_e32 v44, v59
	v_mov_b32_e32 v45, v61
	v_pk_add_f32 v[62:63], v[14:15], v[38:39] op_sel_hi:[1,0] neg_lo:[0,1] neg_hi:[0,1]
	v_pk_add_f32 v[64:65], v[16:17], v[38:39] op_sel_hi:[1,0] neg_lo:[0,1] neg_hi:[0,1]
	v_pk_add_f32 v[66:67], v[18:19], v[38:39] op_sel_hi:[1,0] neg_lo:[0,1] neg_hi:[0,1]
	v_pk_add_f32 v[68:69], v[20:21], v[38:39] op_sel_hi:[1,0] neg_lo:[0,1] neg_hi:[0,1]
	v_mov_b32_e32 v38, v54
	v_mov_b32_e32 v39, v56
	v_mov_b32_e32 v42, v58
	v_mov_b32_e32 v43, v60
	v_pk_mul_f32 v[40:41], v[40:41], v[40:41]
	v_pk_mul_f32 v[44:45], v[44:45], v[44:45]
	v_mul_f32_e32 v46, v62, v62
	v_mul_f32_e32 v48, v64, v64
	v_pk_fma_f32 v[38:39], v[38:39], v[38:39], v[40:41]
	v_pk_fma_f32 v[40:41], v[42:43], v[42:43], v[44:45]
	v_pk_mul_f32 v[50:51], v[66:67], v[66:67]
	v_pk_mul_f32 v[52:53], v[68:69], v[68:69]
	v_pk_fma_f32 v[46:47], v[62:63], v[62:63], v[46:47] op_sel_hi:[1,1,0]
	v_pk_fma_f32 v[48:49], v[64:65], v[64:65], v[48:49] op_sel_hi:[1,1,0]
	v_pk_add_f32 v[38:39], v[38:39], v[38:39] op_sel_hi:[0,1]
	v_pk_add_f32 v[40:41], v[40:41], v[40:41] op_sel_hi:[0,1]
	v_mov_b32_e32 v46, v50
	v_mov_b32_e32 v48, v51
	v_mov_b32_e32 v38, v52
	v_mov_b32_e32 v40, v53
	v_pk_add_f32 v[42:43], v[46:47], v[48:49]
	v_pk_add_f32 v[38:39], v[38:39], v[40:41]
	s_nop 0
	v_pk_add_f32 v[38:39], v[42:43], v[38:39]
	s_nop 0
	v_add_f32_e32 v76, v38, v39
	global_load_dwordx4 v[38:41], v4, s[4:5] offset:2048
	global_load_dwordx4 v[42:45], v4, s[6:7] offset:2048
	global_load_dwordx4 v[46:49], v4, s[4:5] offset:3072
	global_load_dwordx4 v[50:53], v4, s[6:7] offset:3072
	v_mov_b32_e32 v70, v76
	s_waitcnt lgkmcnt(0)
	s_nop 1
	v_permlane32_swap_b32_e32 v76, v70
	v_add_f32_e32 v70, v76, v70
	v_mov_b32_e32 v71, v70
	v_mov_b32_e32 v76, 0x3727c5ac
	s_waitcnt lgkmcnt(0)
	s_nop 1
	v_permlane16_swap_b32_e32 v70, v71
	v_add_f32_e32 v70, v70, v71
	s_waitcnt lgkmcnt(0)
	s_nop 1
	v_add_f32_dpp v70, v70, v70 row_ror:8 row_mask:0xf bank_mask:0xf
	v_lshlrev_b64 v[72:73], 11, v[2:3]
	v_lshl_add_u64 v[72:73], s[8:9], 0, v[72:73]
	s_waitcnt lgkmcnt(0)
	s_nop 1
	v_add_f32_dpp v77, v70, v70 row_ror:4 row_mask:0xf bank_mask:0xf
	v_lshlrev_b64 v[70:71], 12, v[2:3]
	v_lshlrev_b32_e32 v2, 3, v1
	v_lshl_add_u64 v[70:71], s[10:11], 0, v[70:71]
	v_lshl_add_u64 v[4:5], v[70:71], 0, v[4:5]
	s_waitcnt lgkmcnt(0)
	s_nop 1
	v_add_f32_dpp v74, v77, v77 row_ror:2 row_mask:0xf bank_mask:0xf
	global_store_dwordx4 v[4:5], v[6:9], off sc1
	global_store_dwordx4 v[4:5], v[10:13], off offset:1024 sc1
	global_store_dwordx4 v[4:5], v[14:17], off offset:2048 sc1
	global_store_dwordx4 v[4:5], v[18:21], off offset:3072 sc1
	v_lshl_add_u64 v[2:3], v[72:73], 0, v[2:3]
	s_waitcnt lgkmcnt(0)
	s_nop 1
	v_add_f32_dpp v1, v74, v74 row_ror:1 row_mask:0xf bank_mask:0xf
	v_fmac_f32_e32 v76, 0x3a800000, v1
	v_mul_f32_e32 v1, 0x4f800000, v76
	v_cmp_gt_f32_e32 vcc, s3, v76
	s_nop 1
	v_cndmask_b32_e32 v1, v76, v1, vcc
	v_sqrt_f32_e32 v70, v1
	s_nop 0
	v_add_u32_e32 v6, -1, v70
	v_add_u32_e32 v7, 1, v70
	v_fma_f32 v8, -v6, v70, v1
	v_fma_f32 v9, -v7, v70, v1
	v_cmp_ge_f32_e64 s[4:5], 0, v8
	s_nop 1
	v_cndmask_b32_e64 v6, v70, v6, s[4:5]
	v_cmp_lt_f32_e64 s[4:5], 0, v9
	s_nop 1
	v_cndmask_b32_e64 v6, v6, v7, s[4:5]
	v_mul_f32_e32 v7, 0x37800000, v6
	v_cndmask_b32_e32 v6, v6, v7, vcc
	v_cmp_class_f32_e32 vcc, v1, v78
	s_nop 1
	v_cndmask_b32_e32 v1, v6, v1, vcc
	v_div_scale_f32 v6, s[4:5], v1, v1, 1.0
	v_rcp_f32_e32 v7, v6
	v_div_scale_f32 v4, vcc, 1.0, v1, 1.0
	v_fma_f32 v5, -v6, v7, 1.0
	v_fmac_f32_e32 v7, v5, v7
	v_mul_f32_e32 v5, v4, v7
	v_fma_f32 v8, -v6, v5, v4
	v_fmac_f32_e32 v5, v8, v7
	v_fma_f32 v4, -v6, v5, v4
	v_div_fmas_f32 v4, v4, v7, v5
	v_div_fixup_f32 v4, v4, v1, 1.0
	v_pk_mul_f32 v[6:7], v[54:55], v[4:5] op_sel_hi:[1,0]
	v_pk_mul_f32 v[8:9], v[56:57], v[4:5] op_sel_hi:[1,0]
	v_pk_mul_f32 v[10:11], v[58:59], v[4:5] op_sel_hi:[1,0]
	v_pk_mul_f32 v[12:13], v[60:61], v[4:5] op_sel_hi:[1,0]
	v_pk_mul_f32 v[14:15], v[62:63], v[4:5] op_sel_hi:[1,0]
	v_pk_mul_f32 v[16:17], v[64:65], v[4:5] op_sel_hi:[1,0]
	v_pk_mul_f32 v[18:19], v[66:67], v[4:5] op_sel_hi:[1,0]
	v_pk_mul_f32 v[4:5], v[68:69], v[4:5] op_sel_hi:[1,0]
	s_waitcnt vmcnt(10)
	v_pk_fma_f32 v[6:7], v[22:23], v[6:7], v[26:27]
	v_pk_fma_f32 v[8:9], v[24:25], v[8:9], v[28:29]
	s_waitcnt vmcnt(8)
	v_pk_fma_f32 v[10:11], v[30:31], v[10:11], v[34:35]
	v_pk_fma_f32 v[12:13], v[32:33], v[12:13], v[36:37]
	s_waitcnt vmcnt(6)
	v_pk_fma_f32 v[14:15], v[14:15], v[38:39], v[42:43]
	v_pk_fma_f32 v[16:17], v[16:17], v[40:41], v[44:45]
	s_waitcnt vmcnt(4)
	v_pk_fma_f32 v[18:19], v[18:19], v[46:47], v[50:51]
	v_pk_fma_f32 v[4:5], v[4:5], v[48:49], v[52:53]
	v_cvt_pk_f16_f32 v6, v6, v7
	v_cvt_pk_f16_f32 v7, v8, v9
	v_cvt_pk_f16_f32 v8, v10, v11
	v_cvt_pk_f16_f32 v9, v12, v13
	v_cvt_pk_f16_f32 v10, v14, v15
	v_cvt_pk_f16_f32 v11, v16, v17
	v_cvt_pk_f16_f32 v12, v18, v19
	v_cvt_pk_f16_f32 v13, v4, v5
	global_store_dwordx2 v[2:3], v[6:7], off sc1
	global_store_dwordx2 v[2:3], v[8:9], off offset:512 sc1
	global_store_dwordx2 v[2:3], v[10:11], off offset:1024 sc1
	global_store_dwordx2 v[2:3], v[12:13], off offset:1536 sc1
	s_cbranch_execnz .LBB1_2

.LBB1_18:
	s_waitcnt lgkmcnt(0)
	s_mul_i32 s0, s10, s11
	s_abs_i32 s1, s0
	v_cvt_f32_u32_e32 v1, s1
	s_sub_i32 s16, 0, s1
	s_sub_i32 s2, s19, s2
	s_add_i32 s2, s2, s21
	v_rcp_iflag_f32_e32 v1, v1
	s_abs_i32 s11, s2
	s_xor_b32 s3, s2, s0
	s_ashr_i32 s3, s3, 31
	v_mul_f32_e32 v1, 0x4f7ffffe, v1
	v_cvt_u32_f32_e32 v1, v1
	v_lshrrev_b32_e32 v36, 4, v0
	v_lshlrev_b32_e32 v2, 4, v0
	v_and_b32_e32 v34, 0xf0, v2
	v_readfirstlane_b32 s17, v1
	s_mul_i32 s16, s16, s17
	s_mul_hi_u32 s16, s17, s16
	s_add_i32 s17, s17, s16
	s_mul_hi_u32 s16, s11, s17
	s_mul_i32 s17, s16, s1
	s_sub_i32 s11, s11, s17
	s_add_i32 s18, s16, 1
	s_sub_i32 s17, s11, s1
	s_cmp_ge_u32 s11, s1
	s_cselect_b32 s16, s18, s16
	s_cselect_b32 s11, s17, s11
	s_add_i32 s17, s16, 1
	s_cmp_ge_u32 s11, s1
	s_cselect_b32 s1, s17, s16
	s_abs_i32 s11, s10
	v_cvt_f32_u32_e32 v1, s11
	s_xor_b32 s1, s1, s3
	s_sub_i32 s16, 0, s11
	s_sub_i32 s3, s1, s3
	v_rcp_iflag_f32_e32 v1, v1
	s_mul_i32 s0, s3, s0
	s_sub_i32 s0, s2, s0
	s_abs_i32 s2, s0
	v_mul_f32_e32 v1, 0x4f7ffffe, v1
	v_cvt_u32_f32_e32 v1, v1
	s_xor_b32 s1, s0, s10
	s_ashr_i32 s1, s1, 31
	v_mov_b32_e32 v35, 0
	v_readfirstlane_b32 s17, v1
	s_mul_i32 s16, s16, s17
	s_mul_hi_u32 s16, s17, s16
	s_add_i32 s17, s17, s16
	s_mul_hi_u32 s16, s2, s17
	s_mul_i32 s17, s16, s11
	s_sub_i32 s2, s2, s17
	s_add_i32 s18, s16, 1
	s_sub_i32 s17, s2, s11
	s_cmp_ge_u32 s2, s11
	s_cselect_b32 s16, s18, s16
	s_cselect_b32 s2, s17, s2
	s_add_i32 s17, s16, 1
	s_cmp_ge_u32 s2, s11
	s_cselect_b32 s2, s17, s16
	s_xor_b32 s2, s2, s1
	s_sub_i32 s2, s2, s1
	s_mul_i32 s1, s2, s10
	s_ashr_i32 s11, s3, 31
	s_sub_i32 s10, s0, s1
	s_mul_i32 s0, s12, s11
	s_mul_hi_u32 s1, s12, s3
	s_add_i32 s0, s1, s0
	s_mul_i32 s1, s13, s3
	s_add_i32 s1, s0, s1
	s_mul_i32 s0, s12, s3
	s_lshl_b64 s[0:1], s[0:1], 2
	s_add_u32 s4, s4, s0
	s_addc_u32 s12, s5, s1
	s_mul_i32 s0, s14, s11
	s_mul_hi_u32 s1, s14, s3
	s_add_i32 s0, s1, s0
	s_mul_i32 s1, s15, s3
	s_add_i32 s5, s0, s1
	s_lshl_b32 s0, s10, 6
	s_ashr_i32 s1, s0, 31
	s_lshl_b32 s2, s2, 7
	s_lshl_b64 s[10:11], s[0:1], 2
	s_add_u32 s10, s4, s10
	v_or_b32_e32 v1, s2, v36
	s_addc_u32 s11, s12, s11
	v_lshl_add_u64 v[30:31], s[10:11], 0, v[34:35]
	v_mad_i64_i32 v[2:3], s[10:11], v1, s9, 0
	v_lshl_add_u64 v[10:11], v[2:3], 2, v[30:31]
	v_or_b32_e32 v2, 16, v1
	v_mad_i64_i32 v[2:3], s[10:11], v2, s9, 0
	v_lshl_add_u64 v[12:13], v[2:3], 2, v[30:31]
	global_load_dwordx4 v[2:5], v[10:11], off nt
	global_load_dwordx4 v[6:9], v[12:13], off nt
	v_or_b32_e32 v10, 32, v1
	v_mad_i64_i32 v[10:11], s[10:11], v10, s9, 0
	v_lshl_add_u64 v[18:19], v[10:11], 2, v[30:31]
	v_or_b32_e32 v10, 48, v1
	v_mad_i64_i32 v[10:11], s[10:11], v10, s9, 0
	v_lshl_add_u64 v[20:21], v[10:11], 2, v[30:31]
	global_load_dwordx4 v[10:13], v[18:19], off nt
	global_load_dwordx4 v[14:17], v[20:21], off nt
	v_or_b32_e32 v18, 64, v1
	v_mad_i64_i32 v[18:19], s[10:11], v18, s9, 0
	v_lshl_add_u64 v[26:27], v[18:19], 2, v[30:31]
	v_or_b32_e32 v18, 0x50, v1
	v_mad_i64_i32 v[18:19], s[10:11], v18, s9, 0
	v_lshl_add_u64 v[28:29], v[18:19], 2, v[30:31]
	global_load_dwordx4 v[18:21], v[26:27], off nt
	global_load_dwordx4 v[22:25], v[28:29], off nt
	v_or_b32_e32 v26, 0x60, v1
	v_mad_i64_i32 v[26:27], s[10:11], v26, s9, 0
	v_lshl_add_u64 v[26:27], v[26:27], 2, v[30:31]
	v_or_b32_e32 v1, 0x70, v1
	global_load_dwordx4 v[26:29], v[26:27], off nt
	v_mad_i64_i32 v[32:33], s[10:11], v1, s9, 0
	v_lshl_add_u64 v[30:31], v[32:33], 2, v[30:31]
	global_load_dwordx4 v[30:33], v[30:31], off nt
	s_movk_i32 s1, 0x104
	v_mad_u32_u24 v1, v36, s1, v34
	v_lshlrev_b32_e32 v0, 3, v0
	v_add_u32_e32 v34, 0x1040, v1
	v_add_u32_e32 v37, 0x1048, v1
	v_add_u32_e32 v38, 0x2080, v1
	v_add_u32_e32 v39, 0x2088, v1
	v_add_u32_e32 v40, 0x30c0, v1
	v_add_u32_e32 v41, 0x30c8, v1
	v_add_u32_e32 v42, 0x4100, v1
	v_add_u32_e32 v43, 0x4108, v1
	v_add_u32_e32 v44, 0x5140, v1
	v_and_b32_e32 v0, 0x78, v0
	s_mul_i32 s4, s14, s3
	s_lshl_b64 s[4:5], s[4:5], 1
	s_add_u32 s1, s6, s4
	s_addc_u32 s4, s7, s5
	s_ashr_i32 s3, s2, 31
	s_lshl_b64 s[2:3], s[2:3], 1
	s_add_u32 s2, s1, s2
	s_addc_u32 s3, s4, s3
	s_waitcnt vmcnt(7)
	ds_write2_b32 v1, v2, v3 offset1:1
	ds_write2_b32 v1, v4, v5 offset0:2 offset1:3
	s_waitcnt vmcnt(6)
	ds_write2_b32 v34, v6, v7 offset1:1
	ds_write2_b32 v37, v8, v9 offset1:1
	s_waitcnt vmcnt(5)
	ds_write2_b32 v38, v10, v11 offset1:1
	ds_write2_b32 v39, v12, v13 offset1:1
	s_waitcnt vmcnt(4)
	ds_write2_b32 v40, v14, v15 offset1:1
	ds_write2_b32 v41, v16, v17 offset1:1
	s_waitcnt vmcnt(3)
	ds_write2_b32 v42, v18, v19 offset1:1
	ds_write2_b32 v43, v20, v21 offset1:1
	s_waitcnt vmcnt(2)
	ds_write2_b32 v44, v22, v23 offset1:1
	v_add_u32_e32 v2, 0x5148, v1
	ds_write2_b32 v2, v24, v25 offset1:1
	v_add_u32_e32 v2, 0x6180, v1
	v_lshlrev_b32_e32 v34, 1, v0
	v_mul_u32_u24_e32 v0, 0x104, v0
	s_waitcnt vmcnt(1)
	ds_write2_b32 v2, v26, v27 offset1:1
	v_add_u32_e32 v2, 0x6188, v1
	v_lshl_add_u32 v24, v36, 2, v0
	ds_write2_b32 v2, v28, v29 offset1:1
	v_add_u32_e32 v2, 0x71c0, v1
	v_add_u32_e32 v1, 0x71c8, v1
	v_add_u32_e32 v25, 0x400, v24
	s_waitcnt vmcnt(0)
	ds_write2_b32 v2, v30, v31 offset1:1
	ds_write2_b32 v1, v32, v33 offset1:1
	s_waitcnt lgkmcnt(0)
	s_barrier
	ds_read2_b32 v[4:5], v24 offset1:16
	ds_read2_b32 v[6:7], v24 offset0:130 offset1:146
	ds_read2_b32 v[8:9], v25 offset0:4 offset1:20
	ds_read2_b32 v[10:11], v25 offset0:134 offset1:150
	ds_read2_b32 v[12:13], v25 offset0:199 offset1:215
	ds_read2_b32 v[14:15], v25 offset0:69 offset1:85
	ds_read2_b32 v[16:17], v24 offset0:195 offset1:211
	ds_read2_b32 v[18:19], v24 offset0:65 offset1:81
	v_or_b32_e32 v26, s0, v36
	v_lshl_add_u64 v[20:21], s[2:3], 0, v[34:35]
	v_mad_i64_i32 v[22:23], s[0:1], v26, s8, 0
	s_waitcnt lgkmcnt(3)
	v_cvt_pk_f16_f32 v3, v10, v12
	s_waitcnt lgkmcnt(2)
	v_cvt_pk_f16_f32 v2, v8, v14
	s_waitcnt lgkmcnt(1)
	v_cvt_pk_f16_f32 v1, v6, v16
	s_waitcnt lgkmcnt(0)
	v_cvt_pk_f16_f32 v0, v4, v18
	v_lshl_add_u64 v[22:23], v[22:23], 1, v[20:21]
	global_store_dwordx4 v[22:23], v[0:3], off sc1
	v_or_b32_e32 v4, 16, v26
	s_nop 0
	v_cvt_pk_f16_f32 v3, v11, v13
	v_cvt_pk_f16_f32 v2, v9, v15
	v_cvt_pk_f16_f32 v1, v7, v17
	v_cvt_pk_f16_f32 v0, v5, v19
	ds_read2_b32 v[6:7], v24 offset0:32 offset1:48
	ds_read2_b32 v[8:9], v24 offset0:162 offset1:178
	ds_read2_b32 v[10:11], v25 offset0:36 offset1:52
	ds_read2_b32 v[12:13], v25 offset0:166 offset1:182
	ds_read2_b32 v[14:15], v25 offset0:231 offset1:247
	ds_read2_b32 v[16:17], v25 offset0:101 offset1:117
	ds_read2_b32 v[18:19], v24 offset0:227 offset1:243
	ds_read2_b32 v[22:23], v24 offset0:97 offset1:113
	v_mad_i64_i32 v[4:5], s[0:1], v4, s8, 0
	v_lshl_add_u64 v[4:5], v[4:5], 1, v[20:21]
	global_store_dwordx4 v[4:5], v[0:3], off sc1
	v_or_b32_e32 v4, 32, v26
	v_mad_i64_i32 v[4:5], s[0:1], v4, s8, 0
	s_waitcnt lgkmcnt(3)
	v_cvt_pk_f16_f32 v3, v12, v14
	s_waitcnt lgkmcnt(2)
	v_cvt_pk_f16_f32 v2, v10, v16
	s_waitcnt lgkmcnt(1)
	v_cvt_pk_f16_f32 v1, v8, v18
	s_waitcnt lgkmcnt(0)
	v_cvt_pk_f16_f32 v0, v6, v22
	v_lshl_add_u64 v[4:5], v[4:5], 1, v[20:21]
	global_store_dwordx4 v[4:5], v[0:3], off sc1
	v_or_b32_e32 v4, 48, v26
	v_mad_i64_i32 v[4:5], s[0:1], v4, s8, 0
	v_cvt_pk_f16_f32 v3, v13, v15
	v_cvt_pk_f16_f32 v2, v11, v17
	v_cvt_pk_f16_f32 v1, v9, v19
	v_cvt_pk_f16_f32 v0, v7, v23
	v_lshl_add_u64 v[4:5], v[4:5], 1, v[20:21]
	global_store_dwordx4 v[4:5], v[0:3], off sc1
	s_endpgm
	s_endpgm
	s_endpgm
	s_endpgm
	s_endpgm
	s_endpgm
	s_endpgm
	s_endpgm
	s_endpgm
	s_endpgm
	s_endpgm
	s_endpgm
	s_endpgm
	s_endpgm
	s_endpgm
	s_endpgm
	s_endpgm
	s_endpgm
	s_endpgm
	s_endpgm
	s_endpgm
	s_endpgm
	s_endpgm
	s_endpgm
	s_endpgm
	s_endpgm
	s_endpgm
	s_endpgm
	s_endpgm
	s_endpgm
	s_endpgm
	s_endpgm
	s_endpgm
	s_endpgm
	s_endpgm
	s_endpgm
	s_endpgm
	s_endpgm
	s_endpgm
	s_endpgm
	s_endpgm
	s_endpgm
	s_endpgm
	s_endpgm
